# v8 plus merged counted waits in the DSA fast path (one vmcnt per V chunk / K tile, one lgkmcnt per QK tile)
# baseline (speedup 1.0000x reference)
.Lmy_dsa_fast:
	v_addc_co_u32_e32 v45, vcc, 0, v45, vcc
	global_load_dwordx4 v[44:47], v[44:45], off
	s_nop 0
	global_load_dwordx4 v[138:141], v[134:135], off offset:64
	s_waitcnt vmcnt(1)
	v_cndmask_b32_e64 v137, v47, 0, s[38:39]
	v_cndmask_b32_e64 v136, v46, 0, s[38:39]
	v_cndmask_b32_e64 v135, v45, 0, s[38:39]
	v_cndmask_b32_e64 v134, v44, 0, s[38:39]
	s_waitcnt vmcnt(0)
	v_cndmask_b32_e64 v47, v141, 0, s[38:39]
	v_cndmask_b32_e64 v46, v140, 0, s[38:39]
	v_cndmask_b32_e64 v45, v139, 0, s[38:39]
	v_cndmask_b32_e64 v44, v138, 0, s[38:39]
	ds_bpermute_b32 v102, v248, v0
	ds_bpermute_b32 v103, v248, v1
	ds_bpermute_b32 v104, v248, v2
	ds_bpermute_b32 v105, v248, v3
	ds_bpermute_b32 v106, v248, v4
	ds_bpermute_b32 v107, v248, v5
	ds_bpermute_b32 v108, v248, v6
	ds_bpermute_b32 v109, v248, v7
	ds_bpermute_b32 v110, v248, v8
	ds_bpermute_b32 v111, v248, v9
	ds_bpermute_b32 v112, v248, v10
	ds_bpermute_b32 v113, v248, v11
	ds_bpermute_b32 v114, v248, v12
	ds_bpermute_b32 v115, v248, v13
	ds_bpermute_b32 v116, v248, v14
	ds_bpermute_b32 v117, v248, v15
	s_waitcnt lgkmcnt(8)
	v_mfma_f32_16x16x32_bf16 v[140:143], v[102:105], v[134:137], 0
	v_mfma_f32_16x16x32_bf16 v[142:145], v[106:109], v[44:47], v[140:143]
	ds_bpermute_b32 v102, v248, v16
	ds_bpermute_b32 v103, v248, v17
	ds_bpermute_b32 v104, v248, v18
	ds_bpermute_b32 v105, v248, v19
	ds_bpermute_b32 v106, v248, v20
	ds_bpermute_b32 v107, v248, v21
	ds_bpermute_b32 v108, v248, v22
	ds_bpermute_b32 v109, v248, v23
	s_nop 1
	v_pk_mul_f32 v[142:143], v[142:143], s[74:75] op_sel_hi:[1,0]
	v_pk_mul_f32 v[140:141], v[144:145], s[74:75] op_sel_hi:[1,0]
	v_max3_f32 v49, v142, s82, v143
	v_max3_f32 v49, v49, v140, v141
	s_waitcnt lgkmcnt(8)
	v_mfma_f32_16x16x32_bf16 v[154:157], v[110:113], v[134:137], 0
	v_mfma_f32_16x16x32_bf16 v[154:157], v[114:117], v[44:47], v[154:157]
	ds_bpermute_b32 v110, v248, v24
	ds_bpermute_b32 v111, v248, v25
	ds_bpermute_b32 v112, v248, v26
	ds_bpermute_b32 v113, v248, v27
	ds_bpermute_b32 v114, v248, v28
	ds_bpermute_b32 v115, v248, v29
	ds_bpermute_b32 v116, v248, v30
	ds_bpermute_b32 v117, v248, v31
	s_nop 1
	v_pk_mul_f32 v[144:145], v[154:155], s[74:75] op_sel_hi:[1,0]
	v_pk_mul_f32 v[138:139], v[156:157], s[74:75] op_sel_hi:[1,0]
	v_max3_f32 v49, v49, v144, v145
	v_max3_f32 v49, v49, v138, v139
	s_waitcnt lgkmcnt(8)
	v_mfma_f32_16x16x32_bf16 v[156:159], v[102:105], v[134:137], 0
	v_mfma_f32_16x16x32_bf16 v[158:161], v[106:109], v[44:47], v[156:159]
	ds_bpermute_b32 v102, v248, v32
	ds_bpermute_b32 v103, v248, v33
	ds_bpermute_b32 v104, v248, v34
	ds_bpermute_b32 v105, v248, v35
	ds_bpermute_b32 v106, v248, v36
	ds_bpermute_b32 v107, v248, v37
	ds_bpermute_b32 v108, v248, v38
	ds_bpermute_b32 v109, v248, v39
	s_nop 1
	v_pk_mul_f32 v[158:159], v[158:159], s[74:75] op_sel_hi:[1,0]
	v_pk_mul_f32 v[156:157], v[160:161], s[74:75] op_sel_hi:[1,0]
	v_max3_f32 v49, v49, v158, v159
	v_max3_f32 v49, v49, v156, v157
	s_waitcnt lgkmcnt(8)
	v_mfma_f32_16x16x32_bf16 v[160:163], v[110:113], v[134:137], 0
	v_mfma_f32_16x16x32_bf16 v[160:163], v[114:117], v[44:47], v[160:163]
	ds_bpermute_b32 v110, v248, v40
	ds_bpermute_b32 v111, v248, v41
	ds_bpermute_b32 v112, v248, v42
	ds_bpermute_b32 v113, v248, v43
	ds_bpermute_b32 v114, v248, v50
	ds_bpermute_b32 v115, v248, v51
	ds_bpermute_b32 v116, v248, v52
	ds_bpermute_b32 v117, v248, v53
	s_nop 1
	v_pk_mul_f32 v[160:161], v[160:161], s[74:75] op_sel_hi:[1,0]
	v_pk_mul_f32 v[154:155], v[162:163], s[74:75] op_sel_hi:[1,0]
	v_max3_f32 v49, v49, v160, v161
	v_max3_f32 v49, v49, v154, v155
	s_waitcnt lgkmcnt(8)
	v_mfma_f32_16x16x32_bf16 v[164:167], v[102:105], v[134:137], 0
	v_mfma_f32_16x16x32_bf16 v[166:169], v[106:109], v[44:47], v[164:167]
	ds_bpermute_b32 v102, v248, v54
	ds_bpermute_b32 v103, v248, v55
	ds_bpermute_b32 v104, v248, v56
	ds_bpermute_b32 v105, v248, v57
	ds_bpermute_b32 v106, v248, v58
	ds_bpermute_b32 v107, v248, v59
	ds_bpermute_b32 v108, v248, v60
	ds_bpermute_b32 v109, v248, v61
	s_nop 1
	v_pk_mul_f32 v[166:167], v[166:167], s[74:75] op_sel_hi:[1,0]
	v_pk_mul_f32 v[164:165], v[168:169], s[74:75] op_sel_hi:[1,0]
	v_max3_f32 v49, v49, v166, v167
	v_max3_f32 v49, v49, v164, v165
	s_waitcnt lgkmcnt(8)
	v_mfma_f32_16x16x32_bf16 v[168:171], v[110:113], v[134:137], 0
	v_mfma_f32_16x16x32_bf16 v[168:171], v[114:117], v[44:47], v[168:171]
	ds_bpermute_b32 v110, v248, v62
	ds_bpermute_b32 v111, v248, v63
	ds_bpermute_b32 v112, v248, v64
	ds_bpermute_b32 v113, v248, v65
	ds_bpermute_b32 v114, v248, v66
	ds_bpermute_b32 v115, v248, v67
	ds_bpermute_b32 v116, v248, v68
	ds_bpermute_b32 v117, v248, v69
	s_nop 1
	v_pk_mul_f32 v[168:169], v[168:169], s[74:75] op_sel_hi:[1,0]
	v_pk_mul_f32 v[162:163], v[170:171], s[74:75] op_sel_hi:[1,0]
	v_max3_f32 v49, v49, v168, v169
	v_max3_f32 v49, v49, v162, v163
	s_waitcnt lgkmcnt(8)
	v_mfma_f32_16x16x32_bf16 v[172:175], v[102:105], v[134:137], 0
	v_mfma_f32_16x16x32_bf16 v[174:177], v[106:109], v[44:47], v[172:175]
	s_nop 7
	v_pk_mul_f32 v[174:175], v[174:175], s[74:75] op_sel_hi:[1,0]
	v_pk_mul_f32 v[172:173], v[176:177], s[74:75] op_sel_hi:[1,0]
	v_max3_f32 v49, v49, v174, v175
	v_max3_f32 v49, v49, v172, v173
	s_waitcnt lgkmcnt(0)
	v_mfma_f32_16x16x32_bf16 v[176:179], v[110:113], v[134:137], 0
	v_mfma_f32_16x16x32_bf16 v[176:179], v[114:117], v[44:47], v[176:179]
	s_nop 7
	v_pk_mul_f32 v[176:177], v[176:177], s[74:75] op_sel_hi:[1,0]
	v_pk_mul_f32 v[170:171], v[178:179], s[74:75] op_sel_hi:[1,0]
	v_max3_f32 v49, v49, v176, v177
	v_max3_f32 v49, v49, v170, v171
	s_lshl_b32 s6, s6, 9
	s_add_i32 s19, s6, 0
	s_add_i32 s19, s19, 0x20000
	v_lshl_add_u32 v151, v147, 1, s19
	ds_read_u16 v0, v151 offset:256
	ds_read_u16 v8, v151 offset:288
	ds_read_u16 v16, v151 offset:320
	ds_read_u16 v24, v151 offset:352
	ds_read_u16 v32, v151 offset:384
	ds_read_u16 v40, v151 offset:416
	ds_read_u16 v54, v151 offset:448
	ds_read_u16 v62, v151 offset:480
	s_waitcnt lgkmcnt(0)
	v_lshl_or_b32 v4, v0, 8, v246
	global_load_dwordx4 v[0:3], v4, s[50:51]
	global_load_dwordx4 v[4:7], v4, s[50:51] offset:64
	v_lshl_or_b32 v12, v8, 8, v246
	global_load_dwordx4 v[8:11], v12, s[50:51]
	global_load_dwordx4 v[12:15], v12, s[50:51] offset:64
	v_lshl_or_b32 v20, v16, 8, v246
	global_load_dwordx4 v[16:19], v20, s[50:51]
	global_load_dwordx4 v[20:23], v20, s[50:51] offset:64
	v_lshl_or_b32 v28, v24, 8, v246
	global_load_dwordx4 v[24:27], v28, s[50:51]
	global_load_dwordx4 v[28:31], v28, s[50:51] offset:64
	v_lshl_or_b32 v36, v32, 8, v246
	global_load_dwordx4 v[32:35], v36, s[50:51]
	global_load_dwordx4 v[36:39], v36, s[50:51] offset:64
	v_lshl_or_b32 v50, v40, 8, v246
	global_load_dwordx4 v[40:43], v50, s[50:51]
	global_load_dwordx4 v[50:53], v50, s[50:51] offset:64
	v_lshl_or_b32 v58, v54, 8, v246
	global_load_dwordx4 v[54:57], v58, s[50:51]
	global_load_dwordx4 v[58:61], v58, s[50:51] offset:64
	v_lshl_or_b32 v66, v62, 8, v246
	global_load_dwordx4 v[62:65], v66, s[50:51]
	global_load_dwordx4 v[66:69], v66, s[50:51] offset:64
	s_xor_b64 s[6:7], s[44:45], -1
	s_ashr_i32 s53, s52, 31
	s_waitcnt vmcnt(14)
	ds_bpermute_b32 v102, v248, v0
	ds_bpermute_b32 v103, v248, v1
	ds_bpermute_b32 v104, v248, v2
	ds_bpermute_b32 v105, v248, v3
	ds_bpermute_b32 v106, v248, v4
	ds_bpermute_b32 v107, v248, v5
	ds_bpermute_b32 v108, v248, v6
	ds_bpermute_b32 v109, v248, v7
	s_waitcnt vmcnt(12)
	ds_bpermute_b32 v110, v248, v8
	ds_bpermute_b32 v111, v248, v9
	ds_bpermute_b32 v112, v248, v10
	ds_bpermute_b32 v113, v248, v11
	ds_bpermute_b32 v114, v248, v12
	ds_bpermute_b32 v115, v248, v13
	ds_bpermute_b32 v116, v248, v14
	ds_bpermute_b32 v117, v248, v15
	s_waitcnt lgkmcnt(8)
	v_mfma_f32_16x16x32_bf16 v[180:183], v[102:105], v[134:137], 0
	v_mfma_f32_16x16x32_bf16 v[182:185], v[106:109], v[44:47], v[180:183]
	s_waitcnt vmcnt(10)
	ds_bpermute_b32 v102, v248, v16
	ds_bpermute_b32 v103, v248, v17
	ds_bpermute_b32 v104, v248, v18
	ds_bpermute_b32 v105, v248, v19
	ds_bpermute_b32 v106, v248, v20
	ds_bpermute_b32 v107, v248, v21
	ds_bpermute_b32 v108, v248, v22
	ds_bpermute_b32 v109, v248, v23
	s_nop 1
	v_pk_mul_f32 v[182:183], v[182:183], s[74:75] op_sel_hi:[1,0]
	v_pk_mul_f32 v[180:181], v[184:185], s[74:75] op_sel_hi:[1,0]
	v_max3_f32 v49, v49, v182, v183
	v_max3_f32 v49, v49, v180, v181
	s_waitcnt lgkmcnt(8)
	v_mfma_f32_16x16x32_bf16 v[184:187], v[110:113], v[134:137], 0
	v_mfma_f32_16x16x32_bf16 v[184:187], v[114:117], v[44:47], v[184:187]
	s_waitcnt vmcnt(8)
	ds_bpermute_b32 v110, v248, v24
	ds_bpermute_b32 v111, v248, v25
	ds_bpermute_b32 v112, v248, v26
	ds_bpermute_b32 v113, v248, v27
	ds_bpermute_b32 v114, v248, v28
	ds_bpermute_b32 v115, v248, v29
	ds_bpermute_b32 v116, v248, v30
	ds_bpermute_b32 v117, v248, v31
	s_nop 1
	v_pk_mul_f32 v[184:185], v[184:185], s[74:75] op_sel_hi:[1,0]
	v_pk_mul_f32 v[178:179], v[186:187], s[74:75] op_sel_hi:[1,0]
	v_max3_f32 v49, v49, v184, v185
	v_max3_f32 v49, v49, v178, v179
	s_waitcnt lgkmcnt(8)
	v_mfma_f32_16x16x32_bf16 v[188:191], v[102:105], v[134:137], 0
	v_mfma_f32_16x16x32_bf16 v[190:193], v[106:109], v[44:47], v[188:191]
	s_waitcnt vmcnt(6)
	ds_bpermute_b32 v102, v248, v32
	ds_bpermute_b32 v103, v248, v33
	ds_bpermute_b32 v104, v248, v34
	ds_bpermute_b32 v105, v248, v35
	ds_bpermute_b32 v106, v248, v36
	ds_bpermute_b32 v107, v248, v37
	ds_bpermute_b32 v108, v248, v38
	ds_bpermute_b32 v109, v248, v39
	s_nop 1
	v_pk_mul_f32 v[190:191], v[190:191], s[74:75] op_sel_hi:[1,0]
	v_pk_mul_f32 v[188:189], v[192:193], s[74:75] op_sel_hi:[1,0]
	v_max3_f32 v49, v49, v190, v191
	v_max3_f32 v49, v49, v188, v189
	s_waitcnt lgkmcnt(8)
	v_mfma_f32_16x16x32_bf16 v[192:195], v[110:113], v[134:137], 0
	v_mfma_f32_16x16x32_bf16 v[192:195], v[114:117], v[44:47], v[192:195]
	s_waitcnt vmcnt(4)
	ds_bpermute_b32 v110, v248, v40
	ds_bpermute_b32 v111, v248, v41
	ds_bpermute_b32 v112, v248, v42
	ds_bpermute_b32 v113, v248, v43
	ds_bpermute_b32 v114, v248, v50
	ds_bpermute_b32 v115, v248, v51
	ds_bpermute_b32 v116, v248, v52
	ds_bpermute_b32 v117, v248, v53
	s_nop 1
	v_pk_mul_f32 v[192:193], v[192:193], s[74:75] op_sel_hi:[1,0]
	v_pk_mul_f32 v[186:187], v[194:195], s[74:75] op_sel_hi:[1,0]
	v_max3_f32 v49, v49, v192, v193
	v_max3_f32 v49, v49, v186, v187
	s_waitcnt lgkmcnt(8)
	v_mfma_f32_16x16x32_bf16 v[196:199], v[102:105], v[134:137], 0
	v_mfma_f32_16x16x32_bf16 v[196:199], v[106:109], v[44:47], v[196:199]
	s_waitcnt vmcnt(2)
	ds_bpermute_b32 v102, v248, v54
	ds_bpermute_b32 v103, v248, v55
	ds_bpermute_b32 v104, v248, v56
	ds_bpermute_b32 v105, v248, v57
	ds_bpermute_b32 v106, v248, v58
	ds_bpermute_b32 v107, v248, v59
	ds_bpermute_b32 v108, v248, v60
	ds_bpermute_b32 v109, v248, v61
	s_nop 1
	v_pk_mul_f32 v[200:201], v[196:197], s[74:75] op_sel_hi:[1,0]
	v_pk_mul_f32 v[198:199], v[198:199], s[74:75] op_sel_hi:[1,0]
	v_max3_f32 v49, v49, v200, v201
	v_max3_f32 v49, v49, v198, v199
	s_waitcnt lgkmcnt(8)
	v_mfma_f32_16x16x32_bf16 v[194:197], v[110:113], v[134:137], 0
	v_mfma_f32_16x16x32_bf16 v[194:197], v[114:117], v[44:47], v[194:197]
	s_waitcnt vmcnt(0)
	ds_bpermute_b32 v110, v248, v62
	ds_bpermute_b32 v111, v248, v63
	ds_bpermute_b32 v112, v248, v64
	ds_bpermute_b32 v113, v248, v65
	ds_bpermute_b32 v114, v248, v66
	ds_bpermute_b32 v115, v248, v67
	ds_bpermute_b32 v116, v248, v68
	ds_bpermute_b32 v117, v248, v69
	s_nop 1
	v_pk_mul_f32 v[202:203], v[194:195], s[74:75] op_sel_hi:[1,0]
	v_pk_mul_f32 v[194:195], v[196:197], s[74:75] op_sel_hi:[1,0]
	v_max3_f32 v49, v49, v202, v203
	v_max3_f32 v49, v49, v194, v195
	s_waitcnt lgkmcnt(8)
	v_mfma_f32_16x16x32_bf16 v[206:209], v[102:105], v[134:137], 0
	v_mfma_f32_16x16x32_bf16 v[206:209], v[106:109], v[44:47], v[206:209]
	s_nop 7
	v_pk_mul_f32 v[212:213], v[206:207], s[74:75] op_sel_hi:[1,0]
	v_pk_mul_f32 v[210:211], v[208:209], s[74:75] op_sel_hi:[1,0]
	v_max3_f32 v49, v49, v212, v213
	v_max3_f32 v49, v49, v210, v211
	s_waitcnt lgkmcnt(0)
	v_mfma_f32_16x16x32_bf16 v[134:137], v[110:113], v[134:137], 0
	v_mfma_f32_16x16x32_bf16 v[44:47], v[114:117], v[44:47], v[134:137]
	s_nop 7
	v_pk_mul_f32 v[44:45], v[44:45], s[74:75] op_sel_hi:[1,0]
	s_nop 0
	v_max3_f32 v49, v49, v44, v45
	v_pk_mul_f32 v[204:205], v[46:47], s[74:75] op_sel_hi:[1,0]
	s_nop 0
	v_max3_f32 v49, v49, v204, v205
	s_and_b64 vcc, exec, s[44:45]
	s_cbranch_vccz .Lmy_dsa_fast_nk_skip
	ds_read_u16 v0, v251
	ds_read_u16 v8, v251 offset:32
	ds_read_u16 v16, v251 offset:64
	ds_read_u16 v24, v251 offset:96
	ds_read_u16 v32, v251 offset:128
	ds_read_u16 v40, v251 offset:160
	ds_read_u16 v54, v251 offset:192
	ds_read_u16 v62, v251 offset:224
	s_waitcnt lgkmcnt(0)
	v_lshl_or_b32 v4, v0, 8, v246
	global_load_dwordx4 v[0:3], v4, s[50:51]
	global_load_dwordx4 v[4:7], v4, s[50:51] offset:64
	v_lshl_or_b32 v12, v8, 8, v246
	global_load_dwordx4 v[8:11], v12, s[50:51]
	global_load_dwordx4 v[12:15], v12, s[50:51] offset:64
	v_lshl_or_b32 v20, v16, 8, v246
	global_load_dwordx4 v[16:19], v20, s[50:51]
	global_load_dwordx4 v[20:23], v20, s[50:51] offset:64
	v_lshl_or_b32 v28, v24, 8, v246
	global_load_dwordx4 v[24:27], v28, s[50:51]
	global_load_dwordx4 v[28:31], v28, s[50:51] offset:64
	v_lshl_or_b32 v36, v32, 8, v246
	global_load_dwordx4 v[32:35], v36, s[50:51]
	global_load_dwordx4 v[36:39], v36, s[50:51] offset:64
	v_lshl_or_b32 v50, v40, 8, v246
	global_load_dwordx4 v[40:43], v50, s[50:51]
	global_load_dwordx4 v[50:53], v50, s[50:51] offset:64
	v_lshl_or_b32 v58, v54, 8, v246
	global_load_dwordx4 v[54:57], v58, s[50:51]
	global_load_dwordx4 v[58:61], v58, s[50:51] offset:64
	v_lshl_or_b32 v66, v62, 8, v246
	global_load_dwordx4 v[62:65], v66, s[50:51]
	global_load_dwordx4 v[66:69], v66, s[50:51] offset:64
.Lmy_dsa_fast_nk_skip:
	v_lshl_add_u32 v151, v247, 1, s19
	ds_read_u16 v46, v151
	ds_read_u16 v47, v151 offset:16
	ds_read_u16 v126, v151 offset:32
	ds_read_u16 v127, v151 offset:48
	s_waitcnt lgkmcnt(0)
	v_lshl_or_b32 v46, v46, 8, v250
	v_lshl_or_b32 v47, v47, 8, v250
	global_load_dwordx4 v[102:105], v46, s[50:51] offset:128
	global_load_dwordx4 v[110:113], v47, s[50:51] offset:128
	v_lshl_or_b32 v46, v126, 8, v250
	v_lshl_or_b32 v47, v127, 8, v250
	global_load_dwordx4 v[126:129], v46, s[50:51] offset:128
	global_load_dwordx4 v[130:133], v47, s[50:51] offset:128
	ds_read_u16 v46, v151 offset:64
	ds_read_u16 v47, v151 offset:80
	ds_read_u16 v118, v151 offset:96
	ds_read_u16 v119, v151 offset:112
	s_waitcnt lgkmcnt(0)
	v_lshl_or_b32 v46, v46, 8, v250
	v_lshl_or_b32 v47, v47, 8, v250
	global_load_dwordx4 v[86:89], v46, s[50:51] offset:128
	global_load_dwordx4 v[94:97], v47, s[50:51] offset:128
	v_lshl_or_b32 v46, v118, 8, v250
	v_lshl_or_b32 v47, v119, 8, v250
	global_load_dwordx4 v[118:121], v46, s[50:51] offset:128
	global_load_dwordx4 v[122:125], v47, s[50:51] offset:128
	ds_read_u16 v46, v151 offset:128
	ds_read_u16 v47, v151 offset:144
	ds_read_u16 v106, v151 offset:160
	ds_read_u16 v107, v151 offset:176
	s_waitcnt lgkmcnt(0)
	v_lshl_or_b32 v46, v46, 8, v250
	v_lshl_or_b32 v47, v47, 8, v250
	global_load_dwordx4 v[78:81], v46, s[50:51] offset:128
	global_load_dwordx4 v[82:85], v47, s[50:51] offset:128
	v_lshl_or_b32 v46, v106, 8, v250
	v_lshl_or_b32 v47, v107, 8, v250
	global_load_dwordx4 v[106:109], v46, s[50:51] offset:128
	global_load_dwordx4 v[114:117], v47, s[50:51] offset:128
	ds_read_u16 v46, v151 offset:192
	ds_read_u16 v47, v151 offset:208
	ds_read_u16 v90, v151 offset:224
	ds_read_u16 v91, v151 offset:240
	s_waitcnt lgkmcnt(0)
	v_lshl_or_b32 v46, v46, 8, v250
	v_lshl_or_b32 v47, v47, 8, v250
	global_load_dwordx4 v[70:73], v46, s[50:51] offset:128
	global_load_dwordx4 v[74:77], v47, s[50:51] offset:128
	v_lshl_or_b32 v46, v90, 8, v250
	v_lshl_or_b32 v47, v91, 8, v250
	global_load_dwordx4 v[90:93], v46, s[50:51] offset:128
	global_load_dwordx4 v[98:101], v47, s[50:51] offset:128
	v_mov_b32_e32 v46, v49
	s_nop 1
	v_permlane32_swap_b32 v49, v46
	s_nop 1
	s_nop 0
	v_max_f32_e32 v46, v46, v46
	v_max_f32_e32 v47, v49, v49
	v_max_f32_e32 v46, v47, v46
	v_mov_b32_e32 v47, v46
	s_nop 1
	v_permlane16_swap_b32 v46, v47
	s_nop 1
	s_nop 0
	v_max_f32_e32 v47, v47, v47
	v_max_f32_e32 v46, v46, v46
	v_max_f32_e32 v49, v46, v47
	s_mov_b32 s32, 0x3fb8aa3b
	v_mul_f32_e32 v49, 0xbfb8aa3b, v49
	v_fma_f32 v135, v141, s32, v49
	v_fma_f32 v141, v158, s32, v49
	v_exp_f32_e32 v226, v141
	v_fma_f32 v141, v159, s32, v49
	v_exp_f32_e32 v227, v141
	v_fma_f32 v141, v156, s32, v49
	v_exp_f32_e32 v228, v141
	v_fma_f32 v141, v157, s32, v49
	v_exp_f32_e32 v229, v141
	v_fma_f32 v141, v160, s32, v49
	v_exp_f32_e32 v230, v141
	v_fma_f32 v141, v161, s32, v49
	v_exp_f32_e32 v231, v141
	v_fma_f32 v141, v154, s32, v49
	v_exp_f32_e32 v232, v141
	v_fma_f32 v141, v155, s32, v49
	v_exp_f32_e32 v233, v141
	v_fma_f32 v141, v166, s32, v49
	v_exp_f32_e32 v218, v141
	v_fma_f32 v141, v167, s32, v49
	v_exp_f32_e32 v219, v141
	v_fma_f32 v141, v164, s32, v49
	v_exp_f32_e32 v220, v141
	v_fma_f32 v141, v165, s32, v49
	v_exp_f32_e32 v221, v141
	v_fma_f32 v141, v168, s32, v49
	v_exp_f32_e32 v222, v141
	v_fma_f32 v141, v169, s32, v49
	v_exp_f32_e32 v223, v141
	v_fma_f32 v141, v162, s32, v49
	v_exp_f32_e32 v224, v141
	v_fma_f32 v141, v163, s32, v49
	v_exp_f32_e32 v225, v141
	v_fma_f32 v141, v174, s32, v49
	v_exp_f32_e32 v206, v141
	v_fma_f32 v141, v175, s32, v49
	v_exp_f32_e32 v207, v141
	v_fma_f32 v141, v172, s32, v49
	v_fma_f32 v46, v142, s32, v49
	v_exp_f32_e32 v208, v141
	v_fma_f32 v141, v173, s32, v49
	v_fma_f32 v47, v143, s32, v49
	v_exp_f32_e32 v46, v46
	v_fma_f32 v134, v140, s32, v49
	v_exp_f32_e32 v209, v141
	v_fma_f32 v141, v176, s32, v49
	v_exp_f32_e32 v47, v47
	v_exp_f32_e32 v134, v134
	v_exp_f32_e32 v214, v141
	v_fma_f32 v141, v177, s32, v49
	v_exp_f32_e32 v135, v135
	v_add_f32_e32 v136, 0, v46
	v_exp_f32_e32 v215, v141
	v_fma_f32 v141, v170, s32, v49
	v_add_f32_e32 v136, v47, v136
	v_add_f32_e32 v136, v134, v136
	v_exp_f32_e32 v216, v141
	v_fma_f32 v141, v171, s32, v49
	v_add_f32_e32 v140, v135, v136
	v_fma_f32 v136, v144, s32, v49
	v_fma_f32 v137, v145, s32, v49
	v_exp_f32_e32 v217, v141
	v_fma_f32 v141, v182, s32, v49
	v_exp_f32_e32 v136, v136
	v_fma_f32 v138, v138, s32, v49
	v_exp_f32_e32 v137, v137
	v_fma_f32 v139, v139, s32, v49
	v_exp_f32_e32 v182, v141
	v_fma_f32 v141, v183, s32, v49
	v_exp_f32_e32 v138, v138
	v_exp_f32_e32 v139, v139
	v_exp_f32_e32 v183, v141
	v_fma_f32 v141, v180, s32, v49
	v_add_f32_e32 v140, v136, v140
	v_add_f32_e32 v140, v137, v140
	v_exp_f32_e32 v180, v141
	v_fma_f32 v141, v181, s32, v49
	v_add_f32_e32 v140, v138, v140
	v_add_f32_e32 v140, v139, v140
	v_exp_f32_e32 v181, v141
	v_fma_f32 v141, v184, s32, v49
	v_add_f32_e32 v140, v226, v140
	v_add_f32_e32 v140, v227, v140
	v_exp_f32_e32 v184, v141
	v_fma_f32 v141, v185, s32, v49
	v_add_f32_e32 v140, v228, v140
	v_add_f32_e32 v140, v229, v140
	v_exp_f32_e32 v185, v141
	v_fma_f32 v141, v178, s32, v49
	v_add_f32_e32 v140, v230, v140
	v_add_f32_e32 v140, v231, v140
	v_exp_f32_e32 v196, v141
	v_fma_f32 v141, v179, s32, v49
	v_add_f32_e32 v140, v232, v140
	v_add_f32_e32 v140, v233, v140
	v_exp_f32_e32 v197, v141
	v_fma_f32 v141, v190, s32, v49
	v_add_f32_e32 v140, v218, v140
	v_add_f32_e32 v140, v219, v140
	v_exp_f32_e32 v172, v141
	v_fma_f32 v141, v191, s32, v49
	v_add_f32_e32 v140, v220, v140
	v_add_f32_e32 v140, v221, v140
	v_exp_f32_e32 v173, v141
	v_fma_f32 v141, v188, s32, v49
	v_add_f32_e32 v140, v222, v140
	v_add_f32_e32 v140, v223, v140
	v_exp_f32_e32 v174, v141
	v_fma_f32 v141, v189, s32, v49
	v_add_f32_e32 v140, v224, v140
	v_add_f32_e32 v140, v225, v140
	v_exp_f32_e32 v175, v141
	v_fma_f32 v141, v192, s32, v49
	v_add_f32_e32 v140, v206, v140
	v_add_f32_e32 v140, v207, v140
	v_exp_f32_e32 v176, v141
	v_fma_f32 v141, v193, s32, v49
	v_add_f32_e32 v140, v208, v140
	v_add_f32_e32 v140, v209, v140
	v_exp_f32_e32 v177, v141
	v_fma_f32 v141, v186, s32, v49
	v_add_f32_e32 v140, v214, v140
	v_add_f32_e32 v140, v215, v140
	v_exp_f32_e32 v178, v141
	v_fma_f32 v141, v187, s32, v49
	v_add_f32_e32 v140, v216, v140
	v_add_f32_e32 v140, v217, v140
	v_exp_f32_e32 v179, v141
	v_fma_f32 v141, v200, s32, v49
	v_add_f32_e32 v140, v182, v140
	v_add_f32_e32 v140, v183, v140
	v_exp_f32_e32 v164, v141
	v_fma_f32 v141, v201, s32, v49
	v_add_f32_e32 v140, v180, v140
	v_add_f32_e32 v140, v181, v140
	v_exp_f32_e32 v165, v141
	v_fma_f32 v141, v198, s32, v49
	v_add_f32_e32 v140, v184, v140
	v_add_f32_e32 v140, v185, v140
	v_exp_f32_e32 v166, v141
	v_fma_f32 v141, v199, s32, v49
	v_add_f32_e32 v140, v196, v140
	v_add_f32_e32 v140, v197, v140
	v_exp_f32_e32 v167, v141
	v_fma_f32 v141, v202, s32, v49
	v_add_f32_e32 v140, v172, v140
	v_add_f32_e32 v140, v173, v140
	v_exp_f32_e32 v168, v141
	v_fma_f32 v141, v203, s32, v49
	v_add_f32_e32 v140, v174, v140
	v_add_f32_e32 v140, v175, v140
	v_exp_f32_e32 v169, v141
	v_fma_f32 v141, v194, s32, v49
	v_add_f32_e32 v140, v176, v140
	v_add_f32_e32 v140, v177, v140
	v_exp_f32_e32 v170, v141
	v_fma_f32 v141, v195, s32, v49
	v_add_f32_e32 v140, v178, v140
	v_add_f32_e32 v140, v179, v140
	v_exp_f32_e32 v171, v141
	v_fma_f32 v141, v212, s32, v49
	v_add_f32_e32 v140, v164, v140
	v_add_f32_e32 v140, v165, v140
	v_exp_f32_e32 v154, v141
	v_fma_f32 v141, v213, s32, v49
	v_add_f32_e32 v140, v166, v140
	v_add_f32_e32 v140, v167, v140
	v_exp_f32_e32 v155, v141
	v_fma_f32 v141, v210, s32, v49
	v_fma_f32 v44, v44, s32, v49
	v_add_f32_e32 v140, v168, v140
	v_add_f32_e32 v140, v169, v140
	v_exp_f32_e32 v156, v141
	v_fma_f32 v141, v211, s32, v49
	v_exp_f32_e32 v158, v44
	v_fma_f32 v44, v45, s32, v49
	v_add_f32_e32 v140, v170, v140
	v_add_f32_e32 v140, v171, v140
	v_exp_f32_e32 v157, v141
	v_exp_f32_e32 v159, v44
	v_fma_f32 v44, v204, s32, v49
	v_add_f32_e32 v140, v154, v140
	v_add_f32_e32 v140, v155, v140
	v_exp_f32_e32 v160, v44
	v_fma_f32 v44, v205, s32, v49
	v_add_f32_e32 v140, v156, v140
	v_add_f32_e32 v140, v157, v140
	v_exp_f32_e32 v161, v44
	v_add_f32_e32 v44, v158, v140
	v_add_f32_e32 v44, v159, v44
	v_add_f32_e32 v44, v160, v44
	v_add_f32_e32 v44, v161, v44
	v_mov_b32_e32 v45, v44
	s_nop 1
	v_permlane32_swap_b32 v44, v45
	s_nop 1
	s_nop 0
	v_add_f32_e32 v44, v44, v45
	v_mov_b32_e32 v45, v44
	s_nop 1
	v_permlane16_swap_b32 v44, v45
	s_nop 1
	s_nop 0
	v_add_f32_e32 v44, v44, v45
	v_div_scale_f32 v45, s[20:21], v44, v44, 1.0
	v_rcp_f32_e32 v49, v45
	s_nop 0
	v_fma_f32 v140, -v45, v49, 1.0
	v_fmac_f32_e32 v49, v140, v49
	v_div_scale_f32 v140, vcc, 1.0, v44, 1.0
	v_mul_f32_e32 v141, v140, v49
	v_fma_f32 v142, -v45, v141, v140
	v_fmac_f32_e32 v141, v142, v49
	v_fma_f32 v45, -v45, v141, v140
	v_div_fmas_f32 v45, v45, v49, v141
	v_div_fixup_f32 v162, v45, v44, 1.0
	s_waitcnt vmcnt(12)
	ds_write_b128 v252, v[102:105]
	ds_write_b128 v252, v[110:113] offset:1152
	ds_write_b128 v252, v[126:129] offset:2304
	ds_write_b128 v252, v[130:133] offset:3456
	ds_read_u16 v44, v151 offset:256
	ds_read_u16 v45, v151 offset:272
	ds_read_u16 v49, v151 offset:288
	ds_read_u16 v126, v151 offset:304
	s_waitcnt lgkmcnt(0)
	v_lshl_or_b32 v44, v44, 8, v250
	v_lshl_or_b32 v45, v45, 8, v250
	global_load_dwordx4 v[102:105], v44, s[50:51] offset:128
	global_load_dwordx4 v[110:113], v45, s[50:51] offset:128
	v_lshl_or_b32 v44, v49, 8, v250
	v_lshl_or_b32 v45, v126, 8, v250
	global_load_dwordx4 v[126:129], v44, s[50:51] offset:128
	global_load_dwordx4 v[130:133], v45, s[50:51] offset:128
	v_pk_mul_f32 v[44:45], v[162:163], v[46:47] op_sel_hi:[0,1]
	v_pk_mul_f32 v[46:47], v[162:163], v[134:135] op_sel_hi:[0,1]
	v_cvt_pk_bf16_f32 v44, v44, v45
	v_cvt_pk_bf16_f32 v45, v46, v47
	v_pk_mul_f32 v[46:47], v[162:163], v[136:137] op_sel_hi:[0,1]
	v_pk_mul_f32 v[134:135], v[162:163], v[138:139] op_sel_hi:[0,1]
	s_waitcnt lgkmcnt(0)
	v_cvt_pk_bf16_f32 v46, v46, v47
	v_cvt_pk_bf16_f32 v47, v134, v135
	ds_read_b64_tr_b16 v[136:137], v249 offset:2304
	ds_read_b64_tr_b16 v[134:135], v249
	ds_read_b64_tr_b16 v[138:139], v249 offset:32
	ds_read_b64_tr_b16 v[186:187], v249 offset:64
	ds_read_b64_tr_b16 v[190:191], v249 offset:96
	ds_read_b64_tr_b16 v[140:141], v249 offset:2336
	ds_read_b64_tr_b16 v[188:189], v249 offset:2368
	ds_read_b64_tr_b16 v[192:193], v249 offset:2400
	s_waitcnt lgkmcnt(6)
	v_mfma_f32_16x16x32_bf16 v[142:145], v[44:47], v[134:137], 0
	s_waitcnt lgkmcnt(2)
	v_mfma_f32_16x16x32_bf16 v[138:141], v[44:47], v[138:141], 0
	s_waitcnt lgkmcnt(1)
	v_mfma_f32_16x16x32_bf16 v[134:137], v[44:47], v[186:189], 0
	s_waitcnt lgkmcnt(0)
	v_mfma_f32_16x16x32_bf16 v[44:47], v[44:47], v[190:193], 0
	s_waitcnt vmcnt(12)
	ds_write_b128 v252, v[86:89] offset:4608
	ds_write_b128 v252, v[94:97] offset:5760
	ds_write_b128 v252, v[118:121] offset:6912
	ds_write_b128 v252, v[122:125] offset:8064
	ds_read_u16 v49, v151 offset:320
	ds_read_u16 v86, v151 offset:336
	ds_read_u16 v118, v151 offset:352
	ds_read_u16 v119, v151 offset:368
	s_waitcnt lgkmcnt(0)
	v_lshl_or_b32 v49, v49, 8, v250
	v_lshl_or_b32 v94, v86, 8, v250
	global_load_dwordx4 v[86:89], v49, s[50:51] offset:128
	s_nop 0
	global_load_dwordx4 v[94:97], v94, s[50:51] offset:128
	v_lshl_or_b32 v49, v118, 8, v250
	v_lshl_or_b32 v122, v119, 8, v250
	global_load_dwordx4 v[118:121], v49, s[50:51] offset:128
	s_nop 0
	global_load_dwordx4 v[122:125], v122, s[50:51] offset:128
	v_pk_mul_f32 v[186:187], v[162:163], v[226:227] op_sel_hi:[0,1]
	v_pk_mul_f32 v[188:189], v[162:163], v[228:229] op_sel_hi:[0,1]
	v_cvt_pk_bf16_f32 v186, v186, v187
	v_cvt_pk_bf16_f32 v187, v188, v189
	v_pk_mul_f32 v[188:189], v[162:163], v[230:231] op_sel_hi:[0,1]
	v_pk_mul_f32 v[190:191], v[162:163], v[232:233] op_sel_hi:[0,1]
	v_cvt_pk_bf16_f32 v188, v188, v189
	v_cvt_pk_bf16_f32 v189, v190, v191
	s_waitcnt lgkmcnt(0)
	ds_read_b64_tr_b16 v[192:193], v249 offset:6912
	ds_read_b64_tr_b16 v[190:191], v249 offset:4608
	ds_read_b64_tr_b16 v[198:199], v249 offset:4640
	s_waitcnt lgkmcnt(1)
	v_mfma_f32_16x16x32_bf16 v[142:145], v[186:189], v[190:193], v[142:145]
	ds_read_b64_tr_b16 v[200:201], v249 offset:6944
	ds_read_b64_tr_b16 v[190:191], v249 offset:4672
	ds_read_b64_tr_b16 v[192:193], v249 offset:6976
	s_waitcnt lgkmcnt(0)
	v_mfma_f32_16x16x32_bf16 v[134:137], v[186:189], v[190:193], v[134:137]
	ds_read_b64_tr_b16 v[190:191], v249 offset:4704
	ds_read_b64_tr_b16 v[192:193], v249 offset:7008
	v_mfma_f32_16x16x32_bf16 v[138:141], v[186:189], v[198:201], v[138:141]
	s_waitcnt lgkmcnt(0)
	v_mfma_f32_16x16x32_bf16 v[44:47], v[186:189], v[190:193], v[44:47]
	s_waitcnt vmcnt(12)
	ds_write_b128 v252, v[78:81]
	ds_write_b128 v252, v[82:85] offset:1152
	ds_write_b128 v252, v[106:109] offset:2304
	ds_write_b128 v252, v[114:117] offset:3456
	ds_read_u16 v49, v151 offset:384
	ds_read_u16 v78, v151 offset:400
	ds_read_u16 v106, v151 offset:416
	ds_read_u16 v107, v151 offset:432
	s_waitcnt lgkmcnt(0)
	v_lshl_or_b32 v49, v49, 8, v250
	v_lshl_or_b32 v82, v78, 8, v250
	global_load_dwordx4 v[78:81], v49, s[50:51] offset:128
	s_nop 0
	global_load_dwordx4 v[82:85], v82, s[50:51] offset:128
	v_lshl_or_b32 v49, v106, 8, v250
	v_lshl_or_b32 v114, v107, 8, v250
	global_load_dwordx4 v[106:109], v49, s[50:51] offset:128
	s_nop 0
	global_load_dwordx4 v[114:117], v114, s[50:51] offset:128
	v_pk_mul_f32 v[186:187], v[162:163], v[218:219] op_sel_hi:[0,1]
	v_pk_mul_f32 v[188:189], v[162:163], v[220:221] op_sel_hi:[0,1]
	v_cvt_pk_bf16_f32 v186, v186, v187
	v_cvt_pk_bf16_f32 v187, v188, v189
	v_pk_mul_f32 v[188:189], v[162:163], v[222:223] op_sel_hi:[0,1]
	v_pk_mul_f32 v[190:191], v[162:163], v[224:225] op_sel_hi:[0,1]
	v_cvt_pk_bf16_f32 v188, v188, v189
	v_cvt_pk_bf16_f32 v189, v190, v191
	s_waitcnt lgkmcnt(0)
	ds_read_b64_tr_b16 v[192:193], v249 offset:2304
	ds_read_b64_tr_b16 v[190:191], v249
	ds_read_b64_tr_b16 v[198:199], v249 offset:32
	s_waitcnt lgkmcnt(1)
	v_mfma_f32_16x16x32_bf16 v[142:145], v[186:189], v[190:193], v[142:145]
	ds_read_b64_tr_b16 v[200:201], v249 offset:2336
	ds_read_b64_tr_b16 v[190:191], v249 offset:64
	ds_read_b64_tr_b16 v[192:193], v249 offset:2368
	s_waitcnt lgkmcnt(0)
	v_mfma_f32_16x16x32_bf16 v[134:137], v[186:189], v[190:193], v[134:137]
	ds_read_b64_tr_b16 v[190:191], v249 offset:96
	ds_read_b64_tr_b16 v[192:193], v249 offset:2400
	v_mfma_f32_16x16x32_bf16 v[138:141], v[186:189], v[198:201], v[138:141]
	s_waitcnt lgkmcnt(0)
	v_mfma_f32_16x16x32_bf16 v[44:47], v[186:189], v[190:193], v[44:47]
	s_waitcnt vmcnt(12)
	ds_write_b128 v252, v[70:73] offset:4608
	ds_write_b128 v252, v[74:77] offset:5760
	ds_write_b128 v252, v[90:93] offset:6912
	ds_write_b128 v252, v[98:101] offset:8064
	ds_read_u16 v49, v151 offset:448
	ds_read_u16 v70, v151 offset:464
	ds_read_u16 v90, v151 offset:480
	ds_read_u16 v91, v151 offset:496
	s_waitcnt lgkmcnt(0)
	v_lshl_or_b32 v49, v49, 8, v250
	v_lshl_or_b32 v74, v70, 8, v250
	global_load_dwordx4 v[70:73], v49, s[50:51] offset:128
	s_nop 0
	global_load_dwordx4 v[74:77], v74, s[50:51] offset:128
	v_lshl_or_b32 v49, v90, 8, v250
	v_lshl_or_b32 v98, v91, 8, v250
	global_load_dwordx4 v[90:93], v49, s[50:51] offset:128
	s_nop 0
	global_load_dwordx4 v[98:101], v98, s[50:51] offset:128
	v_pk_mul_f32 v[186:187], v[162:163], v[206:207] op_sel_hi:[0,1]
	v_pk_mul_f32 v[188:189], v[162:163], v[208:209] op_sel_hi:[0,1]
	v_cvt_pk_bf16_f32 v186, v186, v187
	v_cvt_pk_bf16_f32 v187, v188, v189
	v_pk_mul_f32 v[188:189], v[162:163], v[214:215] op_sel_hi:[0,1]
	v_pk_mul_f32 v[190:191], v[162:163], v[216:217] op_sel_hi:[0,1]
	v_cvt_pk_bf16_f32 v188, v188, v189
	v_cvt_pk_bf16_f32 v189, v190, v191
	s_waitcnt lgkmcnt(0)
	ds_read_b64_tr_b16 v[192:193], v249 offset:6912
	ds_read_b64_tr_b16 v[190:191], v249 offset:4608
	ds_read_b64_tr_b16 v[198:199], v249 offset:4640
	s_waitcnt lgkmcnt(1)
	v_mfma_f32_16x16x32_bf16 v[142:145], v[186:189], v[190:193], v[142:145]
	ds_read_b64_tr_b16 v[200:201], v249 offset:6944
	ds_read_b64_tr_b16 v[190:191], v249 offset:4672
	ds_read_b64_tr_b16 v[192:193], v249 offset:6976
	s_waitcnt lgkmcnt(0)
	v_mfma_f32_16x16x32_bf16 v[134:137], v[186:189], v[190:193], v[134:137]
	ds_read_b64_tr_b16 v[190:191], v249 offset:4704
	ds_read_b64_tr_b16 v[192:193], v249 offset:7008
	v_mfma_f32_16x16x32_bf16 v[138:141], v[186:189], v[198:201], v[138:141]
	s_waitcnt lgkmcnt(0)
	v_mfma_f32_16x16x32_bf16 v[44:47], v[186:189], v[190:193], v[44:47]
	v_pk_mul_f32 v[182:183], v[162:163], v[182:183] op_sel_hi:[0,1]
	v_pk_mul_f32 v[180:181], v[162:163], v[180:181] op_sel_hi:[0,1]
	v_cvt_pk_bf16_f32 v182, v182, v183
	v_cvt_pk_bf16_f32 v183, v180, v181
	v_pk_mul_f32 v[180:181], v[162:163], v[184:185] op_sel_hi:[0,1]
	s_waitcnt vmcnt(12)
	ds_write_b128 v252, v[102:105]
	ds_write_b128 v252, v[110:113] offset:1152
	ds_write_b128 v252, v[126:129] offset:2304
	ds_write_b128 v252, v[130:133] offset:3456
	v_cvt_pk_bf16_f32 v184, v180, v181
	v_pk_mul_f32 v[180:181], v[162:163], v[196:197] op_sel_hi:[0,1]
	v_cvt_pk_bf16_f32 v185, v180, v181
	s_waitcnt lgkmcnt(0)
	ds_read_b64_tr_b16 v[188:189], v249 offset:2304
	ds_read_b64_tr_b16 v[186:187], v249
	ds_read_b64_tr_b16 v[190:191], v249 offset:32
	s_waitcnt lgkmcnt(1)
	v_mfma_f32_16x16x32_bf16 v[142:145], v[182:185], v[186:189], v[142:145]
	ds_read_b64_tr_b16 v[192:193], v249 offset:2336
	ds_read_b64_tr_b16 v[186:187], v249 offset:64
	ds_read_b64_tr_b16 v[188:189], v249 offset:2368
	s_waitcnt lgkmcnt(0)
	v_mfma_f32_16x16x32_bf16 v[134:137], v[182:185], v[186:189], v[134:137]
	ds_read_b64_tr_b16 v[186:187], v249 offset:96
	ds_read_b64_tr_b16 v[188:189], v249 offset:2400
	v_mfma_f32_16x16x32_bf16 v[138:141], v[182:185], v[190:193], v[138:141]
	s_waitcnt lgkmcnt(0)
	v_mfma_f32_16x16x32_bf16 v[44:47], v[182:185], v[186:189], v[44:47]
	v_pk_mul_f32 v[172:173], v[162:163], v[172:173] op_sel_hi:[0,1]
	v_pk_mul_f32 v[174:175], v[162:163], v[174:175] op_sel_hi:[0,1]
	s_waitcnt vmcnt(8)
	ds_write_b128 v252, v[86:89] offset:4608
	ds_write_b128 v252, v[94:97] offset:5760
	ds_write_b128 v252, v[118:121] offset:6912
	ds_write_b128 v252, v[122:125] offset:8064
	v_cvt_pk_bf16_f32 v172, v172, v173
	v_cvt_pk_bf16_f32 v173, v174, v175
	v_pk_mul_f32 v[174:175], v[162:163], v[176:177] op_sel_hi:[0,1]
	v_pk_mul_f32 v[176:177], v[162:163], v[178:179] op_sel_hi:[0,1]
	v_cvt_pk_bf16_f32 v174, v174, v175
	v_cvt_pk_bf16_f32 v175, v176, v177
	s_waitcnt lgkmcnt(0)
	ds_read_b64_tr_b16 v[178:179], v249 offset:6912
	ds_read_b64_tr_b16 v[176:177], v249 offset:4608
	ds_read_b64_tr_b16 v[180:181], v249 offset:4640
	s_waitcnt lgkmcnt(1)
	v_mfma_f32_16x16x32_bf16 v[142:145], v[172:175], v[176:179], v[142:145]
	ds_read_b64_tr_b16 v[182:183], v249 offset:6944
	ds_read_b64_tr_b16 v[176:177], v249 offset:4672
	ds_read_b64_tr_b16 v[178:179], v249 offset:6976
	s_waitcnt lgkmcnt(0)
	v_mfma_f32_16x16x32_bf16 v[134:137], v[172:175], v[176:179], v[134:137]
	ds_read_b64_tr_b16 v[176:177], v249 offset:4704
	ds_read_b64_tr_b16 v[178:179], v249 offset:7008
	v_mfma_f32_16x16x32_bf16 v[138:141], v[172:175], v[180:183], v[138:141]
	s_waitcnt lgkmcnt(0)
	v_mfma_f32_16x16x32_bf16 v[44:47], v[172:175], v[176:179], v[44:47]
	v_pk_mul_f32 v[164:165], v[162:163], v[164:165] op_sel_hi:[0,1]
	v_pk_mul_f32 v[166:167], v[162:163], v[166:167] op_sel_hi:[0,1]
	s_waitcnt vmcnt(4)
	ds_write_b128 v252, v[78:81]
	ds_write_b128 v252, v[82:85] offset:1152
	ds_write_b128 v252, v[106:109] offset:2304
	ds_write_b128 v252, v[114:117] offset:3456
	v_cvt_pk_bf16_f32 v164, v164, v165
	v_cvt_pk_bf16_f32 v165, v166, v167
	v_pk_mul_f32 v[166:167], v[162:163], v[168:169] op_sel_hi:[0,1]
	v_pk_mul_f32 v[168:169], v[162:163], v[170:171] op_sel_hi:[0,1]
	v_cvt_pk_bf16_f32 v166, v166, v167
	v_cvt_pk_bf16_f32 v167, v168, v169
	s_waitcnt lgkmcnt(0)
	ds_read_b64_tr_b16 v[170:171], v249 offset:2304
	ds_read_b64_tr_b16 v[168:169], v249
	ds_read_b64_tr_b16 v[172:173], v249 offset:32
	s_waitcnt lgkmcnt(1)
	v_mfma_f32_16x16x32_bf16 v[142:145], v[164:167], v[168:171], v[142:145]
	ds_read_b64_tr_b16 v[174:175], v249 offset:2336
	ds_read_b64_tr_b16 v[168:169], v249 offset:64
	ds_read_b64_tr_b16 v[170:171], v249 offset:2368
	s_waitcnt lgkmcnt(0)
	v_mfma_f32_16x16x32_bf16 v[134:137], v[164:167], v[168:171], v[134:137]
	ds_read_b64_tr_b16 v[168:169], v249 offset:96
	ds_read_b64_tr_b16 v[170:171], v249 offset:2400
	v_mfma_f32_16x16x32_bf16 v[138:141], v[164:167], v[172:175], v[138:141]
	s_waitcnt lgkmcnt(0)
	v_mfma_f32_16x16x32_bf16 v[44:47], v[164:167], v[168:171], v[44:47]
	v_pk_mul_f32 v[154:155], v[162:163], v[154:155] op_sel_hi:[0,1]
	v_pk_mul_f32 v[156:157], v[162:163], v[156:157] op_sel_hi:[0,1]
	s_waitcnt vmcnt(0)
	ds_write_b128 v252, v[70:73] offset:4608
	ds_write_b128 v252, v[74:77] offset:5760
	ds_write_b128 v252, v[90:93] offset:6912
	ds_write_b128 v252, v[98:101] offset:8064
	v_cvt_pk_bf16_f32 v154, v154, v155
	v_cvt_pk_bf16_f32 v155, v156, v157
	v_pk_mul_f32 v[156:157], v[162:163], v[158:159] op_sel_hi:[0,1]
	v_pk_mul_f32 v[158:159], v[162:163], v[160:161] op_sel_hi:[0,1]
	v_cvt_pk_bf16_f32 v156, v156, v157
	v_cvt_pk_bf16_f32 v157, v158, v159
	s_waitcnt lgkmcnt(0)
	ds_read_b64_tr_b16 v[160:161], v249 offset:6912
	ds_read_b64_tr_b16 v[158:159], v249 offset:4608
	ds_read_b64_tr_b16 v[162:163], v249 offset:4640
	s_waitcnt lgkmcnt(1)
	v_mfma_f32_16x16x32_bf16 v[142:145], v[154:157], v[158:161], v[142:145]
	ds_read_b64_tr_b16 v[164:165], v249 offset:6944
	ds_read_b64_tr_b16 v[158:159], v249 offset:4672
	ds_read_b64_tr_b16 v[160:161], v249 offset:6976
	s_waitcnt lgkmcnt(0)
	v_mfma_f32_16x16x32_bf16 v[134:137], v[154:157], v[158:161], v[134:137]
	ds_read_b64_tr_b16 v[158:159], v249 offset:4704
	ds_read_b64_tr_b16 v[160:161], v249 offset:7008
	v_mfma_f32_16x16x32_bf16 v[138:141], v[154:157], v[162:165], v[138:141]
	s_waitcnt lgkmcnt(0)
	v_mfma_f32_16x16x32_bf16 v[44:47], v[154:157], v[158:161], v[44:47]
	s_waitcnt lgkmcnt(0)
	s_and_saveexec_b64 s[8:9], s[40:41]
	s_cbranch_execz .LBB0_784
	s_lshl_b64 s[18:19], s[52:53], 10
	v_lshl_add_u64 v[154:155], v[148:149], 0, s[18:19]
	v_cvt_pk_bf16_f32 v49, v142, v143
	global_store_short v[154:155], v49, off
	global_store_short_d16_hi v[154:155], v49, off offset:128
	v_cvt_pk_bf16_f32 v49, v144, v145
	global_store_short v[154:155], v49, off offset:256
	global_store_short_d16_hi v[154:155], v49, off offset:384
	v_cvt_pk_bf16_f32 v49, v138, v139
	global_store_short v[154:155], v49, off offset:32
	global_store_short_d16_hi v[154:155], v49, off offset:160
	v_cvt_pk_bf16_f32 v49, v140, v141
	global_store_short v[154:155], v49, off offset:288
	global_store_short_d16_hi v[154:155], v49, off offset:416
	v_cvt_pk_bf16_f32 v49, v134, v135
	global_store_short v[154:155], v49, off offset:64
	global_store_short_d16_hi v[154:155], v49, off offset:192
	v_cvt_pk_bf16_f32 v49, v136, v137
	global_store_short v[154:155], v49, off offset:320
	global_store_short_d16_hi v[154:155], v49, off offset:448
	v_cvt_pk_bf16_f32 v49, v44, v45
	global_store_short v[154:155], v49, off offset:96
	global_store_short_d16_hi v[154:155], v49, off offset:224
	v_cvt_pk_bf16_f32 v49, v46, v47
	global_store_short v[154:155], v49, off offset:352
	global_store_short_d16_hi v[154:155], v49, off offset:480
	s_branch .LBB0_784
